# expert GEMM epilogues: dropped redundant zero-inits before the fp8 packs; down-projection epilogue reads its 16 slot/weight LDS entries up front instead of one pair per row block with an immediate wai
# speedup vs baseline: 1.0043x; 1.0043x over previous
; #define LAS __attribute__((address_space(3)))
; DI unsigned pk4f8(float a, float b, float c, float d) { int p = __builtin_amdgcn_cvt_pk_fp8_f32(a, b, 0, false); p = __builtin_amdgcn_cvt_pk_fp8_f32(c, d, p, true); return (unsigned)p; }
;     __device__ __forceinline__ void operator()(const f32x4 (&acc)[2][2][4][2], const Unit& u, int wr, int wc, int fr, int fq) const {
;         unsigned char* base = (unsigned char*)u.O; const int acol = u.a1 * 128 + wc * 32 + 8 * fq;
;         const LAS float* bt = (const LAS float*)((LAS unsigned char*)lds_raw + LDS_CTL_OFF + 4096 + u.buf * 1024) + wc * 32 + 8 * fq;
;         const int row0 = wr * 64 + fr;
;         f32x4 bgv[2], buv[2];
; #pragma unroll
;         for (int n = 0; n < 2; ++n) { bgv[n] = *(const LAS f32x4*)(bt + 4 * n); buv[n] = *(const LAS f32x4*)(bt + 128 + 4 * n); }
; #pragma unroll
;         for (int ai = 0; ai < 2; ++ai)
; #pragma unroll
;             for (int m = 0; m < 4; ++m) {
;                 float o[8];
; #pragma unroll
;                 for (int n = 0; n < 2; ++n) { const f32x4 g4 = acc[ai][0][m][n] * WSCALE_INV + bgv[n], u4 = acc[ai][1][m][n] * WSCALE_INV + buv[n];
; #pragma unroll
;                     for (int e = 0; e < 4; e += 2) {
;                         f32x2 g = {fminf(g4[e], 7.0f), fminf(g4[e + 1], 7.0f)}; const f32x2 up = {fminf(fmaxf(u4[e], -7.0f), 7.0f), fminf(fmaxf(u4[e + 1], -7.0f), 7.0f)};
;                         const f32x2 z = g * (-2.4554669595930157f); f32x2 ex; ex.x = __builtin_amdgcn_exp2f(z.x); ex.y = __builtin_amdgcn_exp2f(z.y);
;                         const f32x2 den = ex + 1.0f; f32x2 sg; sg.x = __builtin_amdgcn_rcpf(den.x); sg.y = __builtin_amdgcn_rcpf(den.y);
;                         const f32x2 r = (up + 1.0f) * g * sg; o[4 * n + e] = r.x; o[4 * n + e + 1] = r.y; } }
;                 u32x2 w; w.x = pk4f8(o[0], o[1], o[2], o[3]); w.y = pk4f8(o[4], o[5], o[6], o[7]);
;                 *(u32x2*)(base + (size_t)(row0 + ai * HALF + m * 16) * 2048 + acol) = w; __builtin_amdgcn_sched_barrier(0); }
.LBB0_1254:
	v_mbcnt_lo_u32_b32 v17, -1, 0
	v_mbcnt_hi_u32_b32 v17, -1, v17
	s_lshl_b32 s2, s65, 10
	s_and_b32 s2, s2, 0x400
	v_ashrrev_i32_e32 v0, 1, v17
	v_and_b32_e32 v16, -8, v0
	s_add_i32 s2, s48, s2
	v_lshl_add_u32 v0, v16, 2, s2
	ds_read_b128 v[12:15], v0
	ds_read_b128 v[4:7], v0 offset:16
	ds_read_b128 v[8:11], v0 offset:512
	ds_read_b128 v[0:3], v0 offset:528
	s_lshl_b32 s2, s63, 7
	s_waitcnt lgkmcnt(3)
	v_pk_fma_f32 v[22:23], v[188:189], s[18:19], v[12:13] op_sel_hi:[1,0,1]
	s_or_b32 s2, s2, s47
	v_min_f32_e32 v22, 0x40e00000, v22
	v_min_f32_e32 v23, 0x40e00000, v23
	v_pk_mul_f32 v[26:27], v[22:23], s[20:21] op_sel_hi:[1,0]
	v_add_u32_e32 v16, s2, v16
	v_exp_f32_e32 v26, v26
	v_exp_f32_e32 v27, v27
	v_and_or_b32 v20, v17, 15, s49
	v_ashrrev_i32_e32 v17, 31, v16
	v_lshl_add_u64 v[18:19], s[24:25], 0, v[16:17]
	v_pk_fma_f32 v[16:17], v[190:191], s[18:19], v[14:15] op_sel_hi:[1,0,1]
	v_pk_add_f32 v[26:27], v[26:27], 1.0 op_sel_hi:[1,0]
	v_min_f32_e32 v16, 0x40e00000, v16
	v_min_f32_e32 v17, 0x40e00000, v17
	v_pk_mul_f32 v[30:31], v[16:17], s[20:21] op_sel_hi:[1,0]
	s_waitcnt lgkmcnt(1)
	v_pk_fma_f32 v[28:29], v[184:185], s[18:19], v[8:9] op_sel_hi:[1,0,1]
	v_rcp_f32_e32 v26, v26
	v_rcp_f32_e32 v27, v27
	v_exp_f32_e32 v30, v30
	v_exp_f32_e32 v31, v31
	v_med3_f32 v28, v28, s54, v206
	v_med3_f32 v29, v29, s54, v206
	v_pk_add_f32 v[28:29], v[28:29], 1.0 op_sel_hi:[1,0]
	v_pk_fma_f32 v[24:25], v[186:187], s[18:19], v[10:11] op_sel_hi:[1,0,1]
	v_pk_mul_f32 v[22:23], v[22:23], v[28:29]
	v_med3_f32 v24, v24, s54, v206
	v_pk_mul_f32 v[22:23], v[22:23], v[26:27]
	v_pk_add_f32 v[26:27], v[30:31], 1.0 op_sel_hi:[1,0]
	v_med3_f32 v25, v25, s54, v206
	v_rcp_f32_e32 v26, v26
	v_rcp_f32_e32 v27, v27
	v_pk_add_f32 v[24:25], v[24:25], 1.0 op_sel_hi:[1,0]
	s_waitcnt lgkmcnt(0)
	v_pk_fma_f32 v[32:33], v[176:177], s[18:19], v[0:1] op_sel_hi:[1,0,1]
	v_pk_mul_f32 v[16:17], v[16:17], v[24:25]
	v_pk_fma_f32 v[24:25], v[182:183], s[18:19], v[6:7] op_sel_hi:[1,0,1]
	v_pk_mul_f32 v[16:17], v[16:17], v[26:27]
	v_pk_fma_f32 v[26:27], v[180:181], s[18:19], v[4:5] op_sel_hi:[1,0,1]
	v_med3_f32 v32, v32, s54, v206
	v_min_f32_e32 v26, 0x40e00000, v26
	v_min_f32_e32 v27, 0x40e00000, v27
	v_pk_mul_f32 v[30:31], v[26:27], s[20:21] op_sel_hi:[1,0]
	v_med3_f32 v33, v33, s54, v206
	v_exp_f32_e32 v30, v30
	v_exp_f32_e32 v31, v31
	v_pk_add_f32 v[32:33], v[32:33], 1.0 op_sel_hi:[1,0]
	v_min_f32_e32 v24, 0x40e00000, v24
	v_min_f32_e32 v25, 0x40e00000, v25
	v_pk_add_f32 v[30:31], v[30:31], 1.0 op_sel_hi:[1,0]
	v_pk_mul_f32 v[26:27], v[26:27], v[32:33]
	v_pk_mul_f32 v[32:33], v[24:25], s[20:21] op_sel_hi:[1,0]
	v_rcp_f32_e32 v30, v30
	v_rcp_f32_e32 v31, v31
	v_exp_f32_e32 v32, v32
	v_exp_f32_e32 v33, v33
	v_pk_fma_f32 v[28:29], v[178:179], s[18:19], v[2:3] op_sel_hi:[1,0,1]
	v_pk_mul_f32 v[26:27], v[26:27], v[30:31]
	v_med3_f32 v28, v28, s54, v206
	v_pk_add_f32 v[30:31], v[32:33], 1.0 op_sel_hi:[1,0]
	v_rcp_f32_e32 v30, v30
	v_rcp_f32_e32 v31, v31
	v_med3_f32 v29, v29, s54, v206
	v_cvt_pk_fp8_f32 v32, v22, v23
	v_cvt_pk_fp8_f32 v33, v26, v27
	v_pk_add_f32 v[28:29], v[28:29], 1.0 op_sel_hi:[1,0]
	v_ashrrev_i32_e32 v21, 31, v20
	v_pk_mul_f32 v[22:23], v[24:25], v[28:29]
	v_cvt_pk_fp8_f32 v32, v16, v17 op_sel:[0,0,1]
	v_pk_mul_f32 v[22:23], v[22:23], v[30:31]
	v_lshlrev_b64 v[16:17], 11, v[20:21]
	v_cvt_pk_fp8_f32 v33, v22, v23 op_sel:[0,0,1]
	v_lshl_add_u64 v[16:17], v[18:19], 0, v[16:17]
	global_store_dwordx2 v[16:17], v[32:33], off
	v_pk_fma_f32 v[24:25], v[172:173], s[18:19], v[12:13] op_sel_hi:[1,0,1]
	v_pk_fma_f32 v[22:23], v[174:175], s[18:19], v[14:15] op_sel_hi:[1,0,1]
	v_min_f32_e32 v24, 0x40e00000, v24
	v_min_f32_e32 v25, 0x40e00000, v25
	v_pk_mul_f32 v[28:29], v[24:25], s[20:21] op_sel_hi:[1,0]
	v_min_f32_e32 v22, 0x40e00000, v22
	v_exp_f32_e32 v28, v28
	v_exp_f32_e32 v29, v29
	v_min_f32_e32 v23, 0x40e00000, v23
	v_pk_mul_f32 v[32:33], v[22:23], s[20:21] op_sel_hi:[1,0]
	v_pk_fma_f32 v[30:31], v[168:169], s[18:19], v[8:9] op_sel_hi:[1,0,1]
	v_pk_add_f32 v[28:29], v[28:29], 1.0 op_sel_hi:[1,0]
	v_exp_f32_e32 v32, v32
	v_rcp_f32_e32 v28, v28
	v_rcp_f32_e32 v29, v29
	v_exp_f32_e32 v33, v33
	v_med3_f32 v30, v30, s54, v206
	v_med3_f32 v31, v31, s54, v206
	v_pk_add_f32 v[30:31], v[30:31], 1.0 op_sel_hi:[1,0]
	v_pk_fma_f32 v[26:27], v[170:171], s[18:19], v[10:11] op_sel_hi:[1,0,1]
	v_pk_mul_f32 v[24:25], v[24:25], v[30:31]
	v_med3_f32 v26, v26, s54, v206
	v_pk_mul_f32 v[24:25], v[24:25], v[28:29]
	v_pk_add_f32 v[28:29], v[32:33], 1.0 op_sel_hi:[1,0]
	v_med3_f32 v27, v27, s54, v206
	v_rcp_f32_e32 v28, v28
	v_rcp_f32_e32 v29, v29
	v_pk_add_f32 v[26:27], v[26:27], 1.0 op_sel_hi:[1,0]
	v_pk_fma_f32 v[34:35], v[160:161], s[18:19], v[0:1] op_sel_hi:[1,0,1]
	v_pk_mul_f32 v[22:23], v[22:23], v[26:27]
	v_pk_fma_f32 v[26:27], v[166:167], s[18:19], v[6:7] op_sel_hi:[1,0,1]
	v_pk_mul_f32 v[22:23], v[22:23], v[28:29]
	v_pk_fma_f32 v[28:29], v[164:165], s[18:19], v[4:5] op_sel_hi:[1,0,1]
	v_med3_f32 v34, v34, s54, v206
	v_min_f32_e32 v28, 0x40e00000, v28
	v_min_f32_e32 v29, 0x40e00000, v29
	v_pk_mul_f32 v[32:33], v[28:29], s[20:21] op_sel_hi:[1,0]
	v_med3_f32 v35, v35, s54, v206
	v_exp_f32_e32 v32, v32
	v_exp_f32_e32 v33, v33
	v_pk_add_f32 v[34:35], v[34:35], 1.0 op_sel_hi:[1,0]
	v_min_f32_e32 v26, 0x40e00000, v26
	v_min_f32_e32 v27, 0x40e00000, v27
	v_pk_add_f32 v[32:33], v[32:33], 1.0 op_sel_hi:[1,0]
	v_pk_mul_f32 v[28:29], v[28:29], v[34:35]
	v_pk_mul_f32 v[34:35], v[26:27], s[20:21] op_sel_hi:[1,0]
	v_rcp_f32_e32 v32, v32
	v_rcp_f32_e32 v33, v33
	v_exp_f32_e32 v34, v34
	v_exp_f32_e32 v35, v35
	v_pk_fma_f32 v[30:31], v[162:163], s[18:19], v[2:3] op_sel_hi:[1,0,1]
; #define LAS __attribute__((address_space(3)))
; DI unsigned pk4f8(float a, float b, float c, float d) { int p = __builtin_amdgcn_cvt_pk_fp8_f32(a, b, 0, false); p = __builtin_amdgcn_cvt_pk_fp8_f32(c, d, p, true); return (unsigned)p; }
;     __device__ __forceinline__ void operator()(const f32x4 (&acc)[2][2][4][2], const Unit& u, int wr, int wc, int fr, int fq) const {
;         unsigned char* base = (unsigned char*)u.O; const int acol = u.a1 * 128 + wc * 32 + 8 * fq;
;         const LAS float* bt = (const LAS float*)((LAS unsigned char*)lds_raw + LDS_CTL_OFF + 4096 + u.buf * 1024) + wc * 32 + 8 * fq;
;         const int row0 = wr * 64 + fr;
;         f32x4 bgv[2], buv[2];
; #pragma unroll
;         for (int n = 0; n < 2; ++n) { bgv[n] = *(const LAS f32x4*)(bt + 4 * n); buv[n] = *(const LAS f32x4*)(bt + 128 + 4 * n); }
; #pragma unroll
;         for (int ai = 0; ai < 2; ++ai)
; #pragma unroll
;             for (int m = 0; m < 4; ++m) {
;                 float o[8];
; #pragma unroll
;                 for (int n = 0; n < 2; ++n) { const f32x4 g4 = acc[ai][0][m][n] * WSCALE_INV + bgv[n], u4 = acc[ai][1][m][n] * WSCALE_INV + buv[n];
; #pragma unroll
;                     for (int e = 0; e < 4; e += 2) {
;                         f32x2 g = {fminf(g4[e], 7.0f), fminf(g4[e + 1], 7.0f)}; const f32x2 up = {fminf(fmaxf(u4[e], -7.0f), 7.0f), fminf(fmaxf(u4[e + 1], -7.0f), 7.0f)};
;                         const f32x2 z = g * (-2.4554669595930157f); f32x2 ex; ex.x = __builtin_amdgcn_exp2f(z.x); ex.y = __builtin_amdgcn_exp2f(z.y);
;                         const f32x2 den = ex + 1.0f; f32x2 sg; sg.x = __builtin_amdgcn_rcpf(den.x); sg.y = __builtin_amdgcn_rcpf(den.y);
;                         const f32x2 r = (up + 1.0f) * g * sg; o[4 * n + e] = r.x; o[4 * n + e + 1] = r.y; } }
;                 u32x2 w; w.x = pk4f8(o[0], o[1], o[2], o[3]); w.y = pk4f8(o[4], o[5], o[6], o[7]);
;                 *(u32x2*)(base + (size_t)(row0 + ai * HALF + m * 16) * 2048 + acol) = w; __builtin_amdgcn_sched_barrier(0); }
	v_pk_mul_f32 v[28:29], v[28:29], v[32:33]
	v_med3_f32 v30, v30, s54, v206
	v_pk_add_f32 v[32:33], v[34:35], 1.0 op_sel_hi:[1,0]
	v_rcp_f32_e32 v32, v32
	v_rcp_f32_e32 v33, v33
	v_med3_f32 v31, v31, s54, v206
	v_cvt_pk_fp8_f32 v34, v24, v25
	v_cvt_pk_fp8_f32 v35, v28, v29
	v_pk_add_f32 v[30:31], v[30:31], 1.0 op_sel_hi:[1,0]
	v_cvt_pk_fp8_f32 v34, v22, v23 op_sel:[0,0,1]
	v_pk_mul_f32 v[24:25], v[26:27], v[30:31]
	v_or_b32_e32 v22, 16, v20
	v_pk_mul_f32 v[24:25], v[24:25], v[32:33]
	v_ashrrev_i32_e32 v23, 31, v22
	v_cvt_pk_fp8_f32 v35, v24, v25 op_sel:[0,0,1]
	v_lshlrev_b64 v[22:23], 11, v[22:23]
	v_lshl_add_u64 v[22:23], v[18:19], 0, v[22:23]
	global_store_dwordx2 v[22:23], v[34:35], off
	v_pk_fma_f32 v[24:25], v[156:157], s[18:19], v[12:13] op_sel_hi:[1,0,1]
	v_pk_fma_f32 v[22:23], v[158:159], s[18:19], v[14:15] op_sel_hi:[1,0,1]
	v_min_f32_e32 v24, 0x40e00000, v24
	v_min_f32_e32 v25, 0x40e00000, v25
	v_pk_mul_f32 v[28:29], v[24:25], s[20:21] op_sel_hi:[1,0]
	v_min_f32_e32 v22, 0x40e00000, v22
	v_exp_f32_e32 v28, v28
	v_exp_f32_e32 v29, v29
	v_min_f32_e32 v23, 0x40e00000, v23
	v_pk_mul_f32 v[32:33], v[22:23], s[20:21] op_sel_hi:[1,0]
	v_pk_fma_f32 v[30:31], v[152:153], s[18:19], v[8:9] op_sel_hi:[1,0,1]
	v_pk_add_f32 v[28:29], v[28:29], 1.0 op_sel_hi:[1,0]
	v_exp_f32_e32 v32, v32
	v_rcp_f32_e32 v28, v28
	v_rcp_f32_e32 v29, v29
	v_exp_f32_e32 v33, v33
	v_med3_f32 v30, v30, s54, v206
	v_med3_f32 v31, v31, s54, v206
	v_pk_add_f32 v[30:31], v[30:31], 1.0 op_sel_hi:[1,0]
	v_pk_fma_f32 v[26:27], v[154:155], s[18:19], v[10:11] op_sel_hi:[1,0,1]
	v_pk_mul_f32 v[24:25], v[24:25], v[30:31]
	v_med3_f32 v26, v26, s54, v206
	v_pk_mul_f32 v[24:25], v[24:25], v[28:29]
	v_pk_add_f32 v[28:29], v[32:33], 1.0 op_sel_hi:[1,0]
	v_med3_f32 v27, v27, s54, v206
	v_rcp_f32_e32 v28, v28
	v_rcp_f32_e32 v29, v29
	v_pk_add_f32 v[26:27], v[26:27], 1.0 op_sel_hi:[1,0]
	v_pk_fma_f32 v[34:35], v[144:145], s[18:19], v[0:1] op_sel_hi:[1,0,1]
	v_pk_mul_f32 v[22:23], v[22:23], v[26:27]
	v_pk_fma_f32 v[26:27], v[150:151], s[18:19], v[6:7] op_sel_hi:[1,0,1]
	v_pk_mul_f32 v[22:23], v[22:23], v[28:29]
	v_pk_fma_f32 v[28:29], v[148:149], s[18:19], v[4:5] op_sel_hi:[1,0,1]
	v_med3_f32 v34, v34, s54, v206
	v_min_f32_e32 v28, 0x40e00000, v28
	v_min_f32_e32 v29, 0x40e00000, v29
	v_pk_mul_f32 v[32:33], v[28:29], s[20:21] op_sel_hi:[1,0]
	v_med3_f32 v35, v35, s54, v206
	v_exp_f32_e32 v32, v32
	v_exp_f32_e32 v33, v33
	v_pk_add_f32 v[34:35], v[34:35], 1.0 op_sel_hi:[1,0]
	v_min_f32_e32 v26, 0x40e00000, v26
	v_min_f32_e32 v27, 0x40e00000, v27
	v_pk_add_f32 v[32:33], v[32:33], 1.0 op_sel_hi:[1,0]
	v_pk_mul_f32 v[28:29], v[28:29], v[34:35]
	v_pk_mul_f32 v[34:35], v[26:27], s[20:21] op_sel_hi:[1,0]
	v_rcp_f32_e32 v32, v32
	v_rcp_f32_e32 v33, v33
	v_exp_f32_e32 v34, v34
	v_exp_f32_e32 v35, v35
	v_pk_fma_f32 v[30:31], v[146:147], s[18:19], v[2:3] op_sel_hi:[1,0,1]
	v_pk_mul_f32 v[28:29], v[28:29], v[32:33]
	v_med3_f32 v30, v30, s54, v206
	v_pk_add_f32 v[32:33], v[34:35], 1.0 op_sel_hi:[1,0]
	v_rcp_f32_e32 v32, v32
	v_rcp_f32_e32 v33, v33
	v_med3_f32 v31, v31, s54, v206
	v_cvt_pk_fp8_f32 v34, v24, v25
	v_cvt_pk_fp8_f32 v35, v28, v29
	v_pk_add_f32 v[30:31], v[30:31], 1.0 op_sel_hi:[1,0]
	v_cvt_pk_fp8_f32 v34, v22, v23 op_sel:[0,0,1]
	v_pk_mul_f32 v[24:25], v[26:27], v[30:31]
	v_or_b32_e32 v22, 32, v20
	v_pk_mul_f32 v[24:25], v[24:25], v[32:33]
	v_ashrrev_i32_e32 v23, 31, v22
	v_cvt_pk_fp8_f32 v35, v24, v25 op_sel:[0,0,1]
	v_lshlrev_b64 v[22:23], 11, v[22:23]
	v_lshl_add_u64 v[22:23], v[18:19], 0, v[22:23]
	global_store_dwordx2 v[22:23], v[34:35], off
	v_pk_fma_f32 v[24:25], v[140:141], s[18:19], v[12:13] op_sel_hi:[1,0,1]
	v_pk_fma_f32 v[22:23], v[142:143], s[18:19], v[14:15] op_sel_hi:[1,0,1]
	v_min_f32_e32 v24, 0x40e00000, v24
	v_min_f32_e32 v25, 0x40e00000, v25
	v_pk_mul_f32 v[28:29], v[24:25], s[20:21] op_sel_hi:[1,0]
	v_min_f32_e32 v22, 0x40e00000, v22
	v_exp_f32_e32 v28, v28
	v_exp_f32_e32 v29, v29
	v_min_f32_e32 v23, 0x40e00000, v23
	v_pk_mul_f32 v[32:33], v[22:23], s[20:21] op_sel_hi:[1,0]
	v_pk_fma_f32 v[30:31], v[136:137], s[18:19], v[8:9] op_sel_hi:[1,0,1]
	v_pk_add_f32 v[28:29], v[28:29], 1.0 op_sel_hi:[1,0]
	v_exp_f32_e32 v32, v32
	v_rcp_f32_e32 v28, v28
	v_rcp_f32_e32 v29, v29
	v_exp_f32_e32 v33, v33
	v_med3_f32 v30, v30, s54, v206
	v_med3_f32 v31, v31, s54, v206
	v_pk_add_f32 v[30:31], v[30:31], 1.0 op_sel_hi:[1,0]
	v_pk_fma_f32 v[26:27], v[138:139], s[18:19], v[10:11] op_sel_hi:[1,0,1]
	v_pk_mul_f32 v[24:25], v[24:25], v[30:31]
	v_med3_f32 v26, v26, s54, v206
	v_pk_mul_f32 v[24:25], v[24:25], v[28:29]
	v_pk_add_f32 v[28:29], v[32:33], 1.0 op_sel_hi:[1,0]
	v_med3_f32 v27, v27, s54, v206
	v_rcp_f32_e32 v28, v28
	v_rcp_f32_e32 v29, v29
	v_pk_add_f32 v[26:27], v[26:27], 1.0 op_sel_hi:[1,0]
	v_pk_fma_f32 v[34:35], v[128:129], s[18:19], v[0:1] op_sel_hi:[1,0,1]
	v_pk_mul_f32 v[22:23], v[22:23], v[26:27]
	v_pk_fma_f32 v[26:27], v[134:135], s[18:19], v[6:7] op_sel_hi:[1,0,1]
	v_pk_mul_f32 v[22:23], v[22:23], v[28:29]
	v_pk_fma_f32 v[28:29], v[132:133], s[18:19], v[4:5] op_sel_hi:[1,0,1]
	v_med3_f32 v34, v34, s54, v206
	v_min_f32_e32 v28, 0x40e00000, v28
	v_min_f32_e32 v29, 0x40e00000, v29
	v_pk_mul_f32 v[32:33], v[28:29], s[20:21] op_sel_hi:[1,0]
	v_med3_f32 v35, v35, s54, v206
	v_exp_f32_e32 v32, v32
	v_exp_f32_e32 v33, v33
	v_pk_add_f32 v[34:35], v[34:35], 1.0 op_sel_hi:[1,0]
	v_min_f32_e32 v26, 0x40e00000, v26
	v_min_f32_e32 v27, 0x40e00000, v27
	v_pk_add_f32 v[32:33], v[32:33], 1.0 op_sel_hi:[1,0]
	v_pk_mul_f32 v[28:29], v[28:29], v[34:35]
	v_pk_mul_f32 v[34:35], v[26:27], s[20:21] op_sel_hi:[1,0]
	v_rcp_f32_e32 v32, v32
	v_rcp_f32_e32 v33, v33
	v_exp_f32_e32 v34, v34
; #define LAS __attribute__((address_space(3)))
; DI unsigned pk4f8(float a, float b, float c, float d) { int p = __builtin_amdgcn_cvt_pk_fp8_f32(a, b, 0, false); p = __builtin_amdgcn_cvt_pk_fp8_f32(c, d, p, true); return (unsigned)p; }
;     __device__ __forceinline__ void operator()(const f32x4 (&acc)[2][2][4][2], const Unit& u, int wr, int wc, int fr, int fq) const {
;         unsigned char* base = (unsigned char*)u.O; const int acol = u.a1 * 128 + wc * 32 + 8 * fq;
;         const LAS float* bt = (const LAS float*)((LAS unsigned char*)lds_raw + LDS_CTL_OFF + 4096 + u.buf * 1024) + wc * 32 + 8 * fq;
;         const int row0 = wr * 64 + fr;
;         f32x4 bgv[2], buv[2];
; #pragma unroll
;         for (int n = 0; n < 2; ++n) { bgv[n] = *(const LAS f32x4*)(bt + 4 * n); buv[n] = *(const LAS f32x4*)(bt + 128 + 4 * n); }
; #pragma unroll
;         for (int ai = 0; ai < 2; ++ai)
; #pragma unroll
;             for (int m = 0; m < 4; ++m) {
;                 float o[8];
; #pragma unroll
;                 for (int n = 0; n < 2; ++n) { const f32x4 g4 = acc[ai][0][m][n] * WSCALE_INV + bgv[n], u4 = acc[ai][1][m][n] * WSCALE_INV + buv[n];
; #pragma unroll
;                     for (int e = 0; e < 4; e += 2) {
;                         f32x2 g = {fminf(g4[e], 7.0f), fminf(g4[e + 1], 7.0f)}; const f32x2 up = {fminf(fmaxf(u4[e], -7.0f), 7.0f), fminf(fmaxf(u4[e + 1], -7.0f), 7.0f)};
;                         const f32x2 z = g * (-2.4554669595930157f); f32x2 ex; ex.x = __builtin_amdgcn_exp2f(z.x); ex.y = __builtin_amdgcn_exp2f(z.y);
;                         const f32x2 den = ex + 1.0f; f32x2 sg; sg.x = __builtin_amdgcn_rcpf(den.x); sg.y = __builtin_amdgcn_rcpf(den.y);
;                         const f32x2 r = (up + 1.0f) * g * sg; o[4 * n + e] = r.x; o[4 * n + e + 1] = r.y; } }
;                 u32x2 w; w.x = pk4f8(o[0], o[1], o[2], o[3]); w.y = pk4f8(o[4], o[5], o[6], o[7]);
;                 *(u32x2*)(base + (size_t)(row0 + ai * HALF + m * 16) * 2048 + acol) = w; __builtin_amdgcn_sched_barrier(0); }
	v_exp_f32_e32 v35, v35
	v_pk_fma_f32 v[30:31], v[130:131], s[18:19], v[2:3] op_sel_hi:[1,0,1]
	v_pk_mul_f32 v[28:29], v[28:29], v[32:33]
	v_med3_f32 v30, v30, s54, v206
	v_pk_add_f32 v[32:33], v[34:35], 1.0 op_sel_hi:[1,0]
	v_rcp_f32_e32 v32, v32
	v_rcp_f32_e32 v33, v33
	v_med3_f32 v31, v31, s54, v206
	v_cvt_pk_fp8_f32 v34, v24, v25
	v_cvt_pk_fp8_f32 v35, v28, v29
	v_pk_add_f32 v[30:31], v[30:31], 1.0 op_sel_hi:[1,0]
	v_or_b32_e32 v20, 48, v20
	v_pk_mul_f32 v[24:25], v[26:27], v[30:31]
	v_cvt_pk_fp8_f32 v34, v22, v23 op_sel:[0,0,1]
	v_pk_mul_f32 v[24:25], v[24:25], v[32:33]
	v_ashrrev_i32_e32 v21, 31, v20
	v_cvt_pk_fp8_f32 v35, v24, v25 op_sel:[0,0,1]
	v_lshlrev_b64 v[20:21], 11, v[20:21]
	v_lshl_add_u64 v[18:19], v[18:19], 0, v[20:21]
	global_store_dwordx2 v[18:19], v[34:35], off
	v_pk_fma_f32 v[20:21], v[124:125], s[18:19], v[12:13] op_sel_hi:[1,0,1]
	v_pk_fma_f32 v[18:19], v[126:127], s[18:19], v[14:15] op_sel_hi:[1,0,1]
	v_min_f32_e32 v20, 0x40e00000, v20
	v_min_f32_e32 v21, 0x40e00000, v21
	v_pk_mul_f32 v[24:25], v[20:21], s[20:21] op_sel_hi:[1,0]
	v_min_f32_e32 v18, 0x40e00000, v18
	v_exp_f32_e32 v24, v24
	v_exp_f32_e32 v25, v25
	v_min_f32_e32 v19, 0x40e00000, v19
	v_pk_mul_f32 v[28:29], v[18:19], s[20:21] op_sel_hi:[1,0]
	v_pk_fma_f32 v[26:27], v[120:121], s[18:19], v[8:9] op_sel_hi:[1,0,1]
	v_pk_add_f32 v[24:25], v[24:25], 1.0 op_sel_hi:[1,0]
	v_exp_f32_e32 v28, v28
	v_rcp_f32_e32 v24, v24
	v_rcp_f32_e32 v25, v25
	v_exp_f32_e32 v29, v29
	v_med3_f32 v26, v26, s54, v206
	v_med3_f32 v27, v27, s54, v206
	v_pk_add_f32 v[26:27], v[26:27], 1.0 op_sel_hi:[1,0]
	v_pk_fma_f32 v[22:23], v[122:123], s[18:19], v[10:11] op_sel_hi:[1,0,1]
	v_pk_mul_f32 v[20:21], v[20:21], v[26:27]
	v_med3_f32 v22, v22, s54, v206
	v_pk_mul_f32 v[20:21], v[20:21], v[24:25]
	v_pk_add_f32 v[24:25], v[28:29], 1.0 op_sel_hi:[1,0]
	v_med3_f32 v23, v23, s54, v206
	v_rcp_f32_e32 v24, v24
	v_rcp_f32_e32 v25, v25
	v_pk_add_f32 v[22:23], v[22:23], 1.0 op_sel_hi:[1,0]
	v_pk_fma_f32 v[30:31], v[112:113], s[18:19], v[0:1] op_sel_hi:[1,0,1]
	v_pk_mul_f32 v[18:19], v[18:19], v[22:23]
	v_pk_fma_f32 v[22:23], v[118:119], s[18:19], v[6:7] op_sel_hi:[1,0,1]
	v_pk_mul_f32 v[18:19], v[18:19], v[24:25]
	v_pk_fma_f32 v[24:25], v[116:117], s[18:19], v[4:5] op_sel_hi:[1,0,1]
	v_med3_f32 v30, v30, s54, v206
	v_min_f32_e32 v24, 0x40e00000, v24
	v_min_f32_e32 v25, 0x40e00000, v25
	v_pk_mul_f32 v[28:29], v[24:25], s[20:21] op_sel_hi:[1,0]
	v_med3_f32 v31, v31, s54, v206
	v_exp_f32_e32 v28, v28
	v_exp_f32_e32 v29, v29
	v_pk_add_f32 v[30:31], v[30:31], 1.0 op_sel_hi:[1,0]
	v_min_f32_e32 v22, 0x40e00000, v22
	v_min_f32_e32 v23, 0x40e00000, v23
	v_pk_add_f32 v[28:29], v[28:29], 1.0 op_sel_hi:[1,0]
	v_pk_mul_f32 v[24:25], v[24:25], v[30:31]
	v_pk_mul_f32 v[30:31], v[22:23], s[20:21] op_sel_hi:[1,0]
	v_rcp_f32_e32 v28, v28
	v_rcp_f32_e32 v29, v29
	v_exp_f32_e32 v30, v30
	v_exp_f32_e32 v31, v31
	v_pk_fma_f32 v[26:27], v[114:115], s[18:19], v[2:3] op_sel_hi:[1,0,1]
	v_pk_mul_f32 v[24:25], v[24:25], v[28:29]
	v_med3_f32 v26, v26, s54, v206
	v_pk_add_f32 v[28:29], v[30:31], 1.0 op_sel_hi:[1,0]
	v_rcp_f32_e32 v28, v28
	v_rcp_f32_e32 v29, v29
	v_med3_f32 v27, v27, s54, v206
	v_cvt_pk_fp8_f32 v30, v20, v21
	v_cvt_pk_fp8_f32 v31, v24, v25
	v_pk_add_f32 v[26:27], v[26:27], 1.0 op_sel_hi:[1,0]
	v_cvt_pk_fp8_f32 v30, v18, v19 op_sel:[0,0,1]
	v_pk_mul_f32 v[20:21], v[22:23], v[26:27]
	v_add_co_u32_e32 v18, vcc, s38, v16
	v_pk_mul_f32 v[20:21], v[20:21], v[28:29]
	s_nop 0
	v_addc_co_u32_e32 v19, vcc, 0, v17, vcc
	v_cvt_pk_fp8_f32 v31, v20, v21 op_sel:[0,0,1]
	global_store_dwordx2 v[18:19], v[30:31], off
	v_pk_fma_f32 v[20:21], v[108:109], s[18:19], v[12:13] op_sel_hi:[1,0,1]
	v_pk_fma_f32 v[18:19], v[110:111], s[18:19], v[14:15] op_sel_hi:[1,0,1]
	v_min_f32_e32 v20, 0x40e00000, v20
	v_min_f32_e32 v21, 0x40e00000, v21
	v_pk_mul_f32 v[24:25], v[20:21], s[20:21] op_sel_hi:[1,0]
	v_min_f32_e32 v18, 0x40e00000, v18
	v_exp_f32_e32 v24, v24
	v_exp_f32_e32 v25, v25
	v_min_f32_e32 v19, 0x40e00000, v19
	v_pk_mul_f32 v[28:29], v[18:19], s[20:21] op_sel_hi:[1,0]
	v_pk_fma_f32 v[26:27], v[104:105], s[18:19], v[8:9] op_sel_hi:[1,0,1]
	v_pk_add_f32 v[24:25], v[24:25], 1.0 op_sel_hi:[1,0]
	v_exp_f32_e32 v28, v28
	v_rcp_f32_e32 v24, v24
	v_rcp_f32_e32 v25, v25
	v_exp_f32_e32 v29, v29
	v_med3_f32 v26, v26, s54, v206
	v_med3_f32 v27, v27, s54, v206
	v_pk_add_f32 v[26:27], v[26:27], 1.0 op_sel_hi:[1,0]
	v_pk_fma_f32 v[22:23], v[106:107], s[18:19], v[10:11] op_sel_hi:[1,0,1]
	v_pk_mul_f32 v[20:21], v[20:21], v[26:27]
	v_med3_f32 v22, v22, s54, v206
	v_pk_mul_f32 v[20:21], v[20:21], v[24:25]
	v_pk_add_f32 v[24:25], v[28:29], 1.0 op_sel_hi:[1,0]
	v_med3_f32 v23, v23, s54, v206
	v_rcp_f32_e32 v24, v24
	v_rcp_f32_e32 v25, v25
	v_pk_add_f32 v[22:23], v[22:23], 1.0 op_sel_hi:[1,0]
	v_pk_fma_f32 v[30:31], v[96:97], s[18:19], v[0:1] op_sel_hi:[1,0,1]
	v_pk_mul_f32 v[18:19], v[18:19], v[22:23]
	v_pk_fma_f32 v[22:23], v[102:103], s[18:19], v[6:7] op_sel_hi:[1,0,1]
	v_pk_mul_f32 v[18:19], v[18:19], v[24:25]
	v_pk_fma_f32 v[24:25], v[100:101], s[18:19], v[4:5] op_sel_hi:[1,0,1]
	v_med3_f32 v30, v30, s54, v206
	v_min_f32_e32 v24, 0x40e00000, v24
	v_min_f32_e32 v25, 0x40e00000, v25
	v_pk_mul_f32 v[28:29], v[24:25], s[20:21] op_sel_hi:[1,0]
	v_med3_f32 v31, v31, s54, v206
	v_exp_f32_e32 v28, v28
	v_exp_f32_e32 v29, v29
	v_pk_add_f32 v[30:31], v[30:31], 1.0 op_sel_hi:[1,0]
	v_min_f32_e32 v22, 0x40e00000, v22
	v_min_f32_e32 v23, 0x40e00000, v23
	v_pk_add_f32 v[28:29], v[28:29], 1.0 op_sel_hi:[1,0]
	v_pk_mul_f32 v[24:25], v[24:25], v[30:31]
	v_pk_mul_f32 v[30:31], v[22:23], s[20:21] op_sel_hi:[1,0]
	v_rcp_f32_e32 v28, v28
	v_rcp_f32_e32 v29, v29
; #define LAS __attribute__((address_space(3)))
; #define PG8_BAR __builtin_amdgcn_s_barrier()
;     ...
;         if (!has_next) break;
; #pragma unroll
;         for (int a = 0; a < 2; ++a)
; #pragma unroll
;             for (int b = 0; b < 2; ++b)
; #pragma unroll
;                 for (int m = 0; m < 4; ++m)
; #pragma unroll
;                     for (int n = 0; n < 2; ++n) acc[a][b][m][n] = (f32x4){0.f, 0.f, 0.f, 0.f};
;         cur = nxt; cA = nA; cB = nB; ++ui;
;         if constexpr (ALIGN_EPI) { if (wr == 1) PG8_BAR; }
;     __device__ __forceinline__ void operator()(const f32x4 (&acc)[2][2][4][2], const Unit& u, int wr, int wc, int fr, int fq) const {
;         unsigned char* base = (unsigned char*)u.O; const int acol = u.a1 * 128 + wc * 32 + 8 * fq;
;         const LAS float* bt = (const LAS float*)((LAS unsigned char*)lds_raw + LDS_CTL_OFF + 4096 + u.buf * 1024) + wc * 32 + 8 * fq;
;         const int row0 = wr * 64 + fr;
;         f32x4 bgv[2], buv[2];
; #pragma unroll
;         for (int n = 0; n < 2; ++n) { bgv[n] = *(const LAS f32x4*)(bt + 4 * n); buv[n] = *(const LAS f32x4*)(bt + 128 + 4 * n); }
; #pragma unroll
;         for (int ai = 0; ai < 2; ++ai)
; #pragma unroll
;             for (int m = 0; m < 4; ++m) {
;                 float o[8];
; #pragma unroll
;                 for (int n = 0; n < 2; ++n) { const f32x4 g4 = acc[ai][0][m][n] * WSCALE_INV + bgv[n], u4 = acc[ai][1][m][n] * WSCALE_INV + buv[n];
; #pragma unroll
;                     for (int e = 0; e < 4; e += 2) {
;                         f32x2 g = {fminf(g4[e], 7.0f), fminf(g4[e + 1], 7.0f)}; const f32x2 up = {fminf(fmaxf(u4[e], -7.0f), 7.0f), fminf(fmaxf(u4[e + 1], -7.0f), 7.0f)};
;                         const f32x2 z = g * (-2.4554669595930157f); f32x2 ex; ex.x = __builtin_amdgcn_exp2f(z.x); ex.y = __builtin_amdgcn_exp2f(z.y);
;                         const f32x2 den = ex + 1.0f; f32x2 sg; sg.x = __builtin_amdgcn_rcpf(den.x); sg.y = __builtin_amdgcn_rcpf(den.y);
;                         const f32x2 r = (up + 1.0f) * g * sg; o[4 * n + e] = r.x; o[4 * n + e + 1] = r.y; } }
;                 u32x2 w; w.x = pk4f8(o[0], o[1], o[2], o[3]); w.y = pk4f8(o[4], o[5], o[6], o[7]);
;                 *(u32x2*)(base + (size_t)(row0 + ai * HALF + m * 16) * 2048 + acol) = w; __builtin_amdgcn_sched_barrier(0); }
	v_exp_f32_e32 v30, v30
	v_exp_f32_e32 v31, v31
	v_pk_fma_f32 v[26:27], v[98:99], s[18:19], v[2:3] op_sel_hi:[1,0,1]
	v_pk_mul_f32 v[24:25], v[24:25], v[28:29]
	v_med3_f32 v26, v26, s54, v206
	v_pk_add_f32 v[28:29], v[30:31], 1.0 op_sel_hi:[1,0]
	v_rcp_f32_e32 v28, v28
	v_rcp_f32_e32 v29, v29
	v_med3_f32 v27, v27, s54, v206
	v_cvt_pk_fp8_f32 v30, v20, v21
	v_cvt_pk_fp8_f32 v31, v24, v25
	v_pk_add_f32 v[26:27], v[26:27], 1.0 op_sel_hi:[1,0]
	v_cvt_pk_fp8_f32 v30, v18, v19 op_sel:[0,0,1]
	v_pk_mul_f32 v[20:21], v[22:23], v[26:27]
	v_add_co_u32_e32 v18, vcc, s55, v16
	v_pk_mul_f32 v[20:21], v[20:21], v[28:29]
	s_nop 0
	v_addc_co_u32_e32 v19, vcc, 0, v17, vcc
	v_cvt_pk_fp8_f32 v31, v20, v21 op_sel:[0,0,1]
	global_store_dwordx2 v[18:19], v[30:31], off
	v_pk_fma_f32 v[20:21], v[92:93], s[18:19], v[12:13] op_sel_hi:[1,0,1]
	v_pk_fma_f32 v[18:19], v[94:95], s[18:19], v[14:15] op_sel_hi:[1,0,1]
	v_min_f32_e32 v20, 0x40e00000, v20
	v_min_f32_e32 v21, 0x40e00000, v21
	v_pk_mul_f32 v[24:25], v[20:21], s[20:21] op_sel_hi:[1,0]
	v_min_f32_e32 v18, 0x40e00000, v18
	v_exp_f32_e32 v24, v24
	v_exp_f32_e32 v25, v25
	v_min_f32_e32 v19, 0x40e00000, v19
	v_pk_mul_f32 v[28:29], v[18:19], s[20:21] op_sel_hi:[1,0]
	v_pk_fma_f32 v[26:27], v[88:89], s[18:19], v[8:9] op_sel_hi:[1,0,1]
	v_pk_add_f32 v[24:25], v[24:25], 1.0 op_sel_hi:[1,0]
	v_exp_f32_e32 v28, v28
	v_rcp_f32_e32 v24, v24
	v_rcp_f32_e32 v25, v25
	v_exp_f32_e32 v29, v29
	v_med3_f32 v26, v26, s54, v206
	v_med3_f32 v27, v27, s54, v206
	v_pk_add_f32 v[26:27], v[26:27], 1.0 op_sel_hi:[1,0]
	v_pk_fma_f32 v[22:23], v[90:91], s[18:19], v[10:11] op_sel_hi:[1,0,1]
	v_pk_mul_f32 v[20:21], v[20:21], v[26:27]
	v_med3_f32 v22, v22, s54, v206
	v_pk_mul_f32 v[20:21], v[20:21], v[24:25]
	v_pk_add_f32 v[24:25], v[28:29], 1.0 op_sel_hi:[1,0]
	v_med3_f32 v23, v23, s54, v206
	v_rcp_f32_e32 v24, v24
	v_rcp_f32_e32 v25, v25
	v_pk_add_f32 v[22:23], v[22:23], 1.0 op_sel_hi:[1,0]
	v_pk_fma_f32 v[30:31], v[80:81], s[18:19], v[0:1] op_sel_hi:[1,0,1]
	v_pk_mul_f32 v[18:19], v[18:19], v[22:23]
	v_pk_fma_f32 v[22:23], v[86:87], s[18:19], v[6:7] op_sel_hi:[1,0,1]
	v_pk_mul_f32 v[18:19], v[18:19], v[24:25]
	v_pk_fma_f32 v[24:25], v[84:85], s[18:19], v[4:5] op_sel_hi:[1,0,1]
	v_med3_f32 v30, v30, s54, v206
	v_min_f32_e32 v24, 0x40e00000, v24
	v_min_f32_e32 v25, 0x40e00000, v25
	v_pk_mul_f32 v[28:29], v[24:25], s[20:21] op_sel_hi:[1,0]
	v_med3_f32 v31, v31, s54, v206
	v_exp_f32_e32 v28, v28
	v_exp_f32_e32 v29, v29
	v_pk_add_f32 v[30:31], v[30:31], 1.0 op_sel_hi:[1,0]
	v_min_f32_e32 v22, 0x40e00000, v22
	v_min_f32_e32 v23, 0x40e00000, v23
	v_pk_add_f32 v[28:29], v[28:29], 1.0 op_sel_hi:[1,0]
	v_pk_mul_f32 v[24:25], v[24:25], v[30:31]
	v_pk_mul_f32 v[30:31], v[22:23], s[20:21] op_sel_hi:[1,0]
	v_rcp_f32_e32 v28, v28
	v_rcp_f32_e32 v29, v29
	v_exp_f32_e32 v30, v30
	v_exp_f32_e32 v31, v31
	v_pk_fma_f32 v[26:27], v[82:83], s[18:19], v[2:3] op_sel_hi:[1,0,1]
	v_pk_mul_f32 v[24:25], v[24:25], v[28:29]
	v_med3_f32 v26, v26, s54, v206
	v_pk_add_f32 v[28:29], v[30:31], 1.0 op_sel_hi:[1,0]
	v_rcp_f32_e32 v28, v28
	v_rcp_f32_e32 v29, v29
	v_med3_f32 v27, v27, s54, v206
	v_cvt_pk_fp8_f32 v30, v20, v21
	v_cvt_pk_fp8_f32 v31, v24, v25
	v_pk_add_f32 v[26:27], v[26:27], 1.0 op_sel_hi:[1,0]
	v_cvt_pk_fp8_f32 v30, v18, v19 op_sel:[0,0,1]
	v_pk_mul_f32 v[20:21], v[22:23], v[26:27]
	v_add_co_u32_e32 v18, vcc, s56, v16
	v_pk_mul_f32 v[20:21], v[20:21], v[28:29]
	s_nop 0
	v_addc_co_u32_e32 v19, vcc, 0, v17, vcc
	v_cvt_pk_fp8_f32 v31, v20, v21 op_sel:[0,0,1]
	global_store_dwordx2 v[18:19], v[30:31], off
	v_pk_fma_f32 v[14:15], v[78:79], s[18:19], v[14:15] op_sel_hi:[1,0,1]
	v_pk_fma_f32 v[8:9], v[72:73], s[18:19], v[8:9] op_sel_hi:[1,0,1]
	v_min_f32_e32 v14, 0x40e00000, v14
	v_min_f32_e32 v15, 0x40e00000, v15
	v_pk_mul_f32 v[20:21], v[14:15], s[20:21] op_sel_hi:[1,0]
	v_pk_fma_f32 v[12:13], v[76:77], s[18:19], v[12:13] op_sel_hi:[1,0,1]
	v_exp_f32_e32 v20, v20
	v_exp_f32_e32 v21, v21
	v_med3_f32 v8, v8, s54, v206
	v_med3_f32 v9, v9, s54, v206
	v_min_f32_e32 v12, 0x40e00000, v12
	v_min_f32_e32 v13, 0x40e00000, v13
	v_pk_add_f32 v[8:9], v[8:9], 1.0 op_sel_hi:[1,0]
	v_pk_mul_f32 v[18:19], v[12:13], s[20:21] op_sel_hi:[1,0]
	v_pk_mul_f32 v[8:9], v[12:13], v[8:9]
	v_pk_add_f32 v[12:13], v[20:21], 1.0 op_sel_hi:[1,0]
	v_pk_fma_f32 v[10:11], v[74:75], s[18:19], v[10:11] op_sel_hi:[1,0,1]
	v_rcp_f32_e32 v12, v12
	v_rcp_f32_e32 v13, v13
	v_med3_f32 v10, v10, s54, v206
	v_med3_f32 v11, v11, s54, v206
	v_pk_add_f32 v[10:11], v[10:11], 1.0 op_sel_hi:[1,0]
	v_pk_fma_f32 v[4:5], v[68:69], s[18:19], v[4:5] op_sel_hi:[1,0,1]
	v_pk_mul_f32 v[10:11], v[14:15], v[10:11]
	v_min_f32_e32 v4, 0x40e00000, v4
	v_min_f32_e32 v5, 0x40e00000, v5
	v_pk_mul_f32 v[10:11], v[10:11], v[12:13]
	v_pk_mul_f32 v[12:13], v[4:5], s[20:21] op_sel_hi:[1,0]
	v_pk_fma_f32 v[0:1], v[64:65], s[18:19], v[0:1] op_sel_hi:[1,0,1]
	v_exp_f32_e32 v18, v18
	v_exp_f32_e32 v19, v19
	v_exp_f32_e32 v12, v12
	v_exp_f32_e32 v13, v13
	v_med3_f32 v0, v0, s54, v206
	v_med3_f32 v1, v1, s54, v206
	v_pk_fma_f32 v[6:7], v[70:71], s[18:19], v[6:7] op_sel_hi:[1,0,1]
	v_pk_add_f32 v[0:1], v[0:1], 1.0 op_sel_hi:[1,0]
	v_pk_add_f32 v[18:19], v[18:19], 1.0 op_sel_hi:[1,0]
	v_pk_mul_f32 v[0:1], v[4:5], v[0:1]
	v_min_f32_e32 v4, 0x40e00000, v6
	v_min_f32_e32 v5, 0x40e00000, v7
	v_pk_mul_f32 v[6:7], v[4:5], s[20:21] op_sel_hi:[1,0]
	v_pk_add_f32 v[12:13], v[12:13], 1.0 op_sel_hi:[1,0]
	v_exp_f32_e32 v6, v6
	v_exp_f32_e32 v7, v7
	v_rcp_f32_e32 v18, v18
	v_rcp_f32_e32 v19, v19
	v_rcp_f32_e32 v12, v12
	v_rcp_f32_e32 v13, v13
	v_pk_add_f32 v[6:7], v[6:7], 1.0 op_sel_hi:[1,0]
	v_pk_mul_f32 v[8:9], v[8:9], v[18:19]
	v_pk_fma_f32 v[2:3], v[66:67], s[18:19], v[2:3] op_sel_hi:[1,0,1]
	v_pk_mul_f32 v[0:1], v[0:1], v[12:13]
	v_rcp_f32_e32 v6, v6
	v_rcp_f32_e32 v7, v7
	v_med3_f32 v2, v2, s54, v206
	v_med3_f32 v3, v3, s54, v206
	v_cvt_pk_fp8_f32 v12, v8, v9
	v_cvt_pk_fp8_f32 v13, v0, v1
	v_pk_add_f32 v[2:3], v[2:3], 1.0 op_sel_hi:[1,0]
	v_cvt_pk_fp8_f32 v12, v10, v11 op_sel:[0,0,1]
	v_pk_mul_f32 v[0:1], v[4:5], v[2:3]
	s_nop 0
	v_pk_mul_f32 v[0:1], v[0:1], v[6:7]
	s_nop 0
	v_cvt_pk_fp8_f32 v13, v0, v1 op_sel:[0,0,1]
	v_add_co_u32_e32 v0, vcc, 0x58000, v16
	s_nop 1
	v_addc_co_u32_e32 v1, vcc, 0, v17, vcc
	global_store_dwordx2 v[0:1], v[12:13], off
	s_and_b64 vcc, exec, s[0:1]
	s_mov_b64 s[0:1], -1
	s_cbranch_vccnz .LBB0_1229
	s_andn2_b64 vcc, exec, s[14:15]
	s_cbranch_vccnz .LBB0_1228
	s_barrier
	s_branch .LBB0_1228

; #define LAS __attribute__((address_space(3)))
; DI unsigned pk4f8(float a, float b, float c, float d) { int p = __builtin_amdgcn_cvt_pk_fp8_f32(a, b, 0, false); p = __builtin_amdgcn_cvt_pk_fp8_f32(c, d, p, true); return (unsigned)p; }
;     __device__ __forceinline__ void operator()(const f32x4 (&acc)[2][2][4][2], const Unit& u, int wr, int wc, int fr, int fq) const {
;         const LAS int* slots = (const LAS int*)((LAS unsigned char*)lds_raw + LDS_CTL_OFF + 2048 + u.buf * 1024); const LAS float* wts = (const LAS float*)((LAS unsigned char*)lds_raw + LDS_CTL_OFF + 4096 + u.buf * 1024); const int valid = u.ldc;
;         const int col0 = u.a1 * BM + wc * 32 + 8 * fq; const float* bp = bdn + (size_t)u.a0 * D + col0;
;         f32x4 bv[2][2];
; #pragma unroll
;         for (int bj = 0; bj < 2; ++bj)
; #pragma unroll
;             for (int n = 0; n < 2; ++n) bv[bj][n] = *(const f32x4*)(bp + bj * HALF + 4 * n);
;         const int row0 = wr * 64 + fr;
; #pragma unroll
;         for (int ai = 0; ai < 2; ++ai)
; #pragma unroll
;             for (int m = 0; m < 4; ++m) { const int r = row0 + ai * HALF + m * 16;
;                 if (r < valid) { const int slot = slots[r]; const float w = wts[r]; unsigned char* rowp = ys + (size_t)slot * D + col0;
; #pragma unroll
;                     for (int bj = 0; bj < 2; ++bj) { const f32x4 v0 = (acc[ai][bj][m][0] * WSCALE_INV + bv[bj][0]) * w, v1 = (acc[ai][bj][m][1] * WSCALE_INV + bv[bj][1]) * w;
;                         u32x2 o; o.x = pk4f8(v0[0], v0[1], v0[2], v0[3]); o.y = pk4f8(v1[0], v1[1], v1[2], v1[3]);
;                         *(u32x2*)(rowp + bj * HALF) = o; } } }
.LBB0_1338:
	s_lshl_b32 s2, s2, 10
	v_mbcnt_lo_u32_b32 v158, -1, 0
	v_mbcnt_hi_u32_b32 v158, -1, v158
	s_and_b32 s2, s2, 0x400
	s_add_i32 s4, s2, 0
	s_lshl_b32 s2, s23, 8
	v_and_b32_e32 v128, 48, v158
	v_readlane_b32 s56, v254, 6
	s_or_b32 s2, s2, s42
	s_ashr_i32 s23, s22, 31
	v_readlane_b32 s57, v254, 7
	v_readlane_b32 s58, v254, 8
	v_readlane_b32 s59, v254, 9
	v_readlane_b32 s60, v254, 10
	v_readlane_b32 s61, v254, 11
	s_add_i32 s53, s4, 0x24800
	v_add_u32_e32 v144, s2, v128
	s_lshl_b64 s[2:3], s[22:23], 13
	v_readlane_b32 s62, v254, 12
	v_readlane_b32 s63, v254, 13
	s_mov_b64 s[56:57], s[60:61]
	s_add_u32 s2, s56, s2
	s_addc_u32 s3, s57, s3
	v_ashrrev_i32_e32 v145, 31, v144
	v_lshl_add_u64 v[132:133], v[144:145], 2, s[2:3]
	global_load_dwordx4 v[136:139], v[132:133], off offset:16
	global_load_dwordx4 v[140:143], v[132:133], off
	global_load_dwordx4 v[128:131], v[132:133], off offset:48
	s_nop 0
	global_load_dwordx4 v[132:135], v[132:133], off offset:32
	v_and_or_b32 v160, v158, 15, s43
	s_add_i32 s4, s4, 0x25000
	v_lshlrev_b32_e32 v158, 2, v160
	v_cmp_gt_i32_e32 vcc, s30, v160
	v_add_u32_e32 v159, s53, v158
	v_add_u32_e32 v158, s4, v158
	s_mov_b64 s[58:59], s[62:63]
	ds_read_b32 v170, v159
	ds_read_b32 v171, v158
	ds_read_b32 v172, v159 offset:64
	ds_read_b32 v173, v158 offset:64
	ds_read_b32 v174, v159 offset:128
	ds_read_b32 v175, v158 offset:128
	ds_read_b32 v176, v159 offset:192
	ds_read_b32 v177, v158 offset:192
	ds_read_b32 v178, v159 offset:512
	ds_read_b32 v179, v158 offset:512
	ds_read_b32 v180, v159 offset:576
	ds_read_b32 v181, v158 offset:576
	ds_read_b32 v182, v159 offset:640
	ds_read_b32 v183, v158 offset:640
	ds_read_b32 v184, v159 offset:704
	ds_read_b32 v185, v158 offset:704
	s_and_saveexec_b64 s[2:3], vcc
	s_cbranch_execz .LBB0_1340
	v_mov_b32_e32 v162, v170
	v_mov_b32_e32 v164, v171
	s_waitcnt vmcnt(3)
	v_pk_fma_f32 v[120:121], v[120:121], s[16:17], v[136:137] op_sel_hi:[1,0,1]
	s_waitcnt vmcnt(2)
	v_pk_fma_f32 v[124:125], v[124:125], s[16:17], v[140:141] op_sel_hi:[1,0,1]
	s_waitcnt lgkmcnt(0)
	v_pk_mul_f32 v[120:121], v[120:121], v[164:165] op_sel_hi:[1,0]
	v_pk_mul_f32 v[124:125], v[124:125], v[164:165] op_sel_hi:[1,0]
	v_cvt_pk_fp8_f32 v167, v120, v121
	v_pk_fma_f32 v[120:121], v[122:123], s[16:17], v[138:139] op_sel_hi:[1,0,1]
	s_waitcnt vmcnt(0)
	v_pk_fma_f32 v[116:117], v[116:117], s[16:17], v[132:133] op_sel_hi:[1,0,1]
	v_pk_mul_f32 v[120:121], v[120:121], v[164:165] op_sel_hi:[1,0]
	v_pk_fma_f32 v[112:113], v[112:113], s[16:17], v[128:129] op_sel_hi:[1,0,1]
	v_cvt_pk_fp8_f32 v166, v124, v125
	v_cvt_pk_fp8_f32 v167, v120, v121 op_sel:[0,0,1]
	v_pk_mul_f32 v[116:117], v[116:117], v[164:165] op_sel_hi:[1,0]
	v_pk_mul_f32 v[112:113], v[112:113], v[164:165] op_sel_hi:[1,0]
	v_cvt_pk_fp8_f32 v168, v116, v117
	v_cvt_pk_fp8_f32 v169, v112, v113
	v_pk_fma_f32 v[126:127], v[126:127], s[16:17], v[142:143] op_sel_hi:[1,0,1]
	v_pk_fma_f32 v[118:119], v[118:119], s[16:17], v[134:135] op_sel_hi:[1,0,1]
	v_pk_mul_f32 v[126:127], v[126:127], v[164:165] op_sel_hi:[1,0]
	v_pk_fma_f32 v[112:113], v[114:115], s[16:17], v[130:131] op_sel_hi:[1,0,1]
	v_ashrrev_i32_e32 v163, 31, v162
	v_cvt_pk_fp8_f32 v166, v126, v127 op_sel:[0,0,1]
	v_pk_mul_f32 v[118:119], v[118:119], v[164:165] op_sel_hi:[1,0]
	v_pk_mul_f32 v[112:113], v[112:113], v[164:165] op_sel_hi:[1,0]
	v_lshlrev_b64 v[162:163], 11, v[162:163]
	v_cvt_pk_fp8_f32 v168, v118, v119 op_sel:[0,0,1]
	v_cvt_pk_fp8_f32 v169, v112, v113 op_sel:[0,0,1]
	v_lshl_add_u64 v[112:113], s[12:13], 0, v[162:163]
	v_lshl_add_u64 v[112:113], v[112:113], 0, v[144:145]
	global_store_dwordx4 v[112:113], v[166:169], off
.LBB0_1340:
	s_or_b64 exec, exec, s[2:3]
	v_or_b32_e32 v112, 16, v160
	v_cmp_gt_i32_e32 vcc, s30, v112
	s_and_saveexec_b64 s[2:3], vcc
	s_cbranch_execz .LBB0_1342
	v_mov_b32_e32 v112, v172
	v_mov_b32_e32 v114, v173
	v_pk_fma_f32 v[104:105], v[104:105], s[16:17], v[136:137] op_sel_hi:[1,0,1]
	v_pk_fma_f32 v[108:109], v[108:109], s[16:17], v[140:141] op_sel_hi:[1,0,1]
	v_pk_mul_f32 v[104:105], v[104:105], v[114:115] op_sel_hi:[1,0]
	v_pk_mul_f32 v[108:109], v[108:109], v[114:115] op_sel_hi:[1,0]
	v_cvt_pk_fp8_f32 v167, v104, v105
	v_pk_fma_f32 v[104:105], v[106:107], s[16:17], v[138:139] op_sel_hi:[1,0,1]
	v_pk_fma_f32 v[100:101], v[100:101], s[16:17], v[132:133] op_sel_hi:[1,0,1]
	v_pk_mul_f32 v[104:105], v[104:105], v[114:115] op_sel_hi:[1,0]
	v_pk_fma_f32 v[96:97], v[96:97], s[16:17], v[128:129] op_sel_hi:[1,0,1]
	v_cvt_pk_fp8_f32 v166, v108, v109
	v_cvt_pk_fp8_f32 v167, v104, v105 op_sel:[0,0,1]
	v_pk_mul_f32 v[100:101], v[100:101], v[114:115] op_sel_hi:[1,0]
	v_pk_mul_f32 v[96:97], v[96:97], v[114:115] op_sel_hi:[1,0]
	v_cvt_pk_fp8_f32 v168, v100, v101
	v_cvt_pk_fp8_f32 v169, v96, v97
	v_pk_fma_f32 v[110:111], v[110:111], s[16:17], v[142:143] op_sel_hi:[1,0,1]
	v_pk_fma_f32 v[102:103], v[102:103], s[16:17], v[134:135] op_sel_hi:[1,0,1]
	v_pk_mul_f32 v[110:111], v[110:111], v[114:115] op_sel_hi:[1,0]
	v_pk_fma_f32 v[96:97], v[98:99], s[16:17], v[130:131] op_sel_hi:[1,0,1]
	v_ashrrev_i32_e32 v113, 31, v112
	v_cvt_pk_fp8_f32 v166, v110, v111 op_sel:[0,0,1]
	v_pk_mul_f32 v[102:103], v[102:103], v[114:115] op_sel_hi:[1,0]
	v_pk_mul_f32 v[96:97], v[96:97], v[114:115] op_sel_hi:[1,0]
	v_lshlrev_b64 v[112:113], 11, v[112:113]
	v_cvt_pk_fp8_f32 v168, v102, v103 op_sel:[0,0,1]
	v_cvt_pk_fp8_f32 v169, v96, v97 op_sel:[0,0,1]
	v_lshl_add_u64 v[96:97], s[12:13], 0, v[112:113]
	v_lshl_add_u64 v[96:97], v[96:97], 0, v[144:145]
	global_store_dwordx4 v[96:97], v[166:169], off
; #define LAS __attribute__((address_space(3)))
; DI unsigned pk4f8(float a, float b, float c, float d) { int p = __builtin_amdgcn_cvt_pk_fp8_f32(a, b, 0, false); p = __builtin_amdgcn_cvt_pk_fp8_f32(c, d, p, true); return (unsigned)p; }
;     __device__ __forceinline__ void operator()(const f32x4 (&acc)[2][2][4][2], const Unit& u, int wr, int wc, int fr, int fq) const {
;         const LAS int* slots = (const LAS int*)((LAS unsigned char*)lds_raw + LDS_CTL_OFF + 2048 + u.buf * 1024); const LAS float* wts = (const LAS float*)((LAS unsigned char*)lds_raw + LDS_CTL_OFF + 4096 + u.buf * 1024); const int valid = u.ldc;
;         const int col0 = u.a1 * BM + wc * 32 + 8 * fq; const float* bp = bdn + (size_t)u.a0 * D + col0;
;         f32x4 bv[2][2];
; #pragma unroll
;         for (int bj = 0; bj < 2; ++bj)
; #pragma unroll
;             for (int n = 0; n < 2; ++n) bv[bj][n] = *(const f32x4*)(bp + bj * HALF + 4 * n);
;         const int row0 = wr * 64 + fr;
; #pragma unroll
;         for (int ai = 0; ai < 2; ++ai)
; #pragma unroll
;             for (int m = 0; m < 4; ++m) { const int r = row0 + ai * HALF + m * 16;
;                 if (r < valid) { const int slot = slots[r]; const float w = wts[r]; unsigned char* rowp = ys + (size_t)slot * D + col0;
; #pragma unroll
;                     for (int bj = 0; bj < 2; ++bj) { const f32x4 v0 = (acc[ai][bj][m][0] * WSCALE_INV + bv[bj][0]) * w, v1 = (acc[ai][bj][m][1] * WSCALE_INV + bv[bj][1]) * w;
;                         u32x2 o; o.x = pk4f8(v0[0], v0[1], v0[2], v0[3]); o.y = pk4f8(v1[0], v1[1], v1[2], v1[3]);
;                         *(u32x2*)(rowp + bj * HALF) = o; } } }
.LBB0_1342:
	s_or_b64 exec, exec, s[2:3]
	v_or_b32_e32 v96, 32, v160
	v_cmp_gt_i32_e32 vcc, s30, v96
	s_and_saveexec_b64 s[2:3], vcc
	s_cbranch_execz .LBB0_1344
	v_mov_b32_e32 v96, v174
	v_mov_b32_e32 v98, v175
	v_pk_fma_f32 v[88:89], v[88:89], s[16:17], v[136:137] op_sel_hi:[1,0,1]
	v_pk_fma_f32 v[92:93], v[92:93], s[16:17], v[140:141] op_sel_hi:[1,0,1]
	v_pk_mul_f32 v[88:89], v[88:89], v[98:99] op_sel_hi:[1,0]
	v_pk_mul_f32 v[92:93], v[92:93], v[98:99] op_sel_hi:[1,0]
	v_cvt_pk_fp8_f32 v167, v88, v89
	v_pk_fma_f32 v[88:89], v[90:91], s[16:17], v[138:139] op_sel_hi:[1,0,1]
	v_pk_fma_f32 v[84:85], v[84:85], s[16:17], v[132:133] op_sel_hi:[1,0,1]
	v_pk_mul_f32 v[88:89], v[88:89], v[98:99] op_sel_hi:[1,0]
	v_pk_fma_f32 v[80:81], v[80:81], s[16:17], v[128:129] op_sel_hi:[1,0,1]
	v_cvt_pk_fp8_f32 v166, v92, v93
	v_cvt_pk_fp8_f32 v167, v88, v89 op_sel:[0,0,1]
	v_pk_mul_f32 v[84:85], v[84:85], v[98:99] op_sel_hi:[1,0]
	v_pk_mul_f32 v[80:81], v[80:81], v[98:99] op_sel_hi:[1,0]
	v_cvt_pk_fp8_f32 v168, v84, v85
	v_cvt_pk_fp8_f32 v169, v80, v81
	v_pk_fma_f32 v[94:95], v[94:95], s[16:17], v[142:143] op_sel_hi:[1,0,1]
	v_pk_fma_f32 v[86:87], v[86:87], s[16:17], v[134:135] op_sel_hi:[1,0,1]
	v_pk_mul_f32 v[94:95], v[94:95], v[98:99] op_sel_hi:[1,0]
	v_pk_fma_f32 v[80:81], v[82:83], s[16:17], v[130:131] op_sel_hi:[1,0,1]
	v_ashrrev_i32_e32 v97, 31, v96
	v_cvt_pk_fp8_f32 v166, v94, v95 op_sel:[0,0,1]
	v_pk_mul_f32 v[86:87], v[86:87], v[98:99] op_sel_hi:[1,0]
	v_pk_mul_f32 v[80:81], v[80:81], v[98:99] op_sel_hi:[1,0]
	v_lshlrev_b64 v[96:97], 11, v[96:97]
	v_cvt_pk_fp8_f32 v168, v86, v87 op_sel:[0,0,1]
	v_cvt_pk_fp8_f32 v169, v80, v81 op_sel:[0,0,1]
	v_lshl_add_u64 v[80:81], s[12:13], 0, v[96:97]
	v_lshl_add_u64 v[80:81], v[80:81], 0, v[144:145]
	global_store_dwordx4 v[80:81], v[166:169], off
.LBB0_1344:
	s_or_b64 exec, exec, s[2:3]
	v_or_b32_e32 v80, 48, v160
	v_cmp_gt_i32_e32 vcc, s30, v80
	s_and_saveexec_b64 s[2:3], vcc
	s_cbranch_execz .LBB0_1346
	v_mov_b32_e32 v80, v176
	v_mov_b32_e32 v82, v177
	v_pk_fma_f32 v[72:73], v[72:73], s[16:17], v[136:137] op_sel_hi:[1,0,1]
	v_pk_fma_f32 v[76:77], v[76:77], s[16:17], v[140:141] op_sel_hi:[1,0,1]
	v_pk_mul_f32 v[72:73], v[72:73], v[82:83] op_sel_hi:[1,0]
	v_pk_mul_f32 v[76:77], v[76:77], v[82:83] op_sel_hi:[1,0]
	v_cvt_pk_fp8_f32 v167, v72, v73
	v_pk_fma_f32 v[72:73], v[74:75], s[16:17], v[138:139] op_sel_hi:[1,0,1]
	v_pk_fma_f32 v[68:69], v[68:69], s[16:17], v[132:133] op_sel_hi:[1,0,1]
	v_pk_mul_f32 v[72:73], v[72:73], v[82:83] op_sel_hi:[1,0]
	v_pk_fma_f32 v[64:65], v[64:65], s[16:17], v[128:129] op_sel_hi:[1,0,1]
	v_cvt_pk_fp8_f32 v166, v76, v77
	v_cvt_pk_fp8_f32 v167, v72, v73 op_sel:[0,0,1]
	v_pk_mul_f32 v[68:69], v[68:69], v[82:83] op_sel_hi:[1,0]
	v_pk_mul_f32 v[64:65], v[64:65], v[82:83] op_sel_hi:[1,0]
	v_cvt_pk_fp8_f32 v168, v68, v69
	v_cvt_pk_fp8_f32 v169, v64, v65
	v_pk_fma_f32 v[78:79], v[78:79], s[16:17], v[142:143] op_sel_hi:[1,0,1]
	v_pk_fma_f32 v[70:71], v[70:71], s[16:17], v[134:135] op_sel_hi:[1,0,1]
	v_pk_mul_f32 v[78:79], v[78:79], v[82:83] op_sel_hi:[1,0]
	v_pk_fma_f32 v[64:65], v[66:67], s[16:17], v[130:131] op_sel_hi:[1,0,1]
	v_ashrrev_i32_e32 v81, 31, v80
	v_cvt_pk_fp8_f32 v166, v78, v79 op_sel:[0,0,1]
	v_pk_mul_f32 v[70:71], v[70:71], v[82:83] op_sel_hi:[1,0]
	v_pk_mul_f32 v[64:65], v[64:65], v[82:83] op_sel_hi:[1,0]
	v_lshlrev_b64 v[80:81], 11, v[80:81]
	v_cvt_pk_fp8_f32 v168, v70, v71 op_sel:[0,0,1]
	v_cvt_pk_fp8_f32 v169, v64, v65 op_sel:[0,0,1]
	v_lshl_add_u64 v[64:65], s[12:13], 0, v[80:81]
	v_lshl_add_u64 v[64:65], v[64:65], 0, v[144:145]
	global_store_dwordx4 v[64:65], v[166:169], off
.LBB0_1346:
	s_or_b64 exec, exec, s[2:3]
	v_add_u32_e32 v64, 0x80, v160
	v_cmp_gt_i32_e32 vcc, s30, v64
	s_and_saveexec_b64 s[2:3], vcc
	s_cbranch_execz .LBB0_1348
	v_mov_b32_e32 v64, v178
	v_mov_b32_e32 v66, v179
	v_pk_fma_f32 v[56:57], v[56:57], s[16:17], v[136:137] op_sel_hi:[1,0,1]
	v_pk_fma_f32 v[60:61], v[60:61], s[16:17], v[140:141] op_sel_hi:[1,0,1]
	v_pk_mul_f32 v[56:57], v[56:57], v[66:67] op_sel_hi:[1,0]
	v_pk_mul_f32 v[60:61], v[60:61], v[66:67] op_sel_hi:[1,0]
	v_cvt_pk_fp8_f32 v167, v56, v57
	v_pk_fma_f32 v[56:57], v[58:59], s[16:17], v[138:139] op_sel_hi:[1,0,1]
	v_pk_fma_f32 v[52:53], v[52:53], s[16:17], v[132:133] op_sel_hi:[1,0,1]
	v_pk_mul_f32 v[56:57], v[56:57], v[66:67] op_sel_hi:[1,0]
	v_pk_fma_f32 v[48:49], v[48:49], s[16:17], v[128:129] op_sel_hi:[1,0,1]
	v_cvt_pk_fp8_f32 v166, v60, v61
	v_cvt_pk_fp8_f32 v167, v56, v57 op_sel:[0,0,1]
	v_pk_mul_f32 v[52:53], v[52:53], v[66:67] op_sel_hi:[1,0]
	v_pk_mul_f32 v[48:49], v[48:49], v[66:67] op_sel_hi:[1,0]
	v_cvt_pk_fp8_f32 v168, v52, v53
	v_cvt_pk_fp8_f32 v169, v48, v49
	v_pk_fma_f32 v[62:63], v[62:63], s[16:17], v[142:143] op_sel_hi:[1,0,1]
	v_pk_fma_f32 v[54:55], v[54:55], s[16:17], v[134:135] op_sel_hi:[1,0,1]
	v_pk_mul_f32 v[62:63], v[62:63], v[66:67] op_sel_hi:[1,0]
	v_pk_fma_f32 v[48:49], v[50:51], s[16:17], v[130:131] op_sel_hi:[1,0,1]
	v_ashrrev_i32_e32 v65, 31, v64
	v_cvt_pk_fp8_f32 v166, v62, v63 op_sel:[0,0,1]
	v_pk_mul_f32 v[54:55], v[54:55], v[66:67] op_sel_hi:[1,0]
	v_pk_mul_f32 v[48:49], v[48:49], v[66:67] op_sel_hi:[1,0]
	v_lshlrev_b64 v[64:65], 11, v[64:65]
	v_cvt_pk_fp8_f32 v168, v54, v55 op_sel:[0,0,1]
	v_cvt_pk_fp8_f32 v169, v48, v49 op_sel:[0,0,1]
	v_lshl_add_u64 v[48:49], s[12:13], 0, v[64:65]
	v_lshl_add_u64 v[48:49], v[48:49], 0, v[144:145]
	global_store_dwordx4 v[48:49], v[166:169], off
; #define LAS __attribute__((address_space(3)))
; DI unsigned pk4f8(float a, float b, float c, float d) { int p = __builtin_amdgcn_cvt_pk_fp8_f32(a, b, 0, false); p = __builtin_amdgcn_cvt_pk_fp8_f32(c, d, p, true); return (unsigned)p; }
;     __device__ __forceinline__ void operator()(const f32x4 (&acc)[2][2][4][2], const Unit& u, int wr, int wc, int fr, int fq) const {
;         const LAS int* slots = (const LAS int*)((LAS unsigned char*)lds_raw + LDS_CTL_OFF + 2048 + u.buf * 1024); const LAS float* wts = (const LAS float*)((LAS unsigned char*)lds_raw + LDS_CTL_OFF + 4096 + u.buf * 1024); const int valid = u.ldc;
;         const int col0 = u.a1 * BM + wc * 32 + 8 * fq; const float* bp = bdn + (size_t)u.a0 * D + col0;
;         f32x4 bv[2][2];
; #pragma unroll
;         for (int bj = 0; bj < 2; ++bj)
; #pragma unroll
;             for (int n = 0; n < 2; ++n) bv[bj][n] = *(const f32x4*)(bp + bj * HALF + 4 * n);
;         const int row0 = wr * 64 + fr;
; #pragma unroll
;         for (int ai = 0; ai < 2; ++ai)
; #pragma unroll
;             for (int m = 0; m < 4; ++m) { const int r = row0 + ai * HALF + m * 16;
;                 if (r < valid) { const int slot = slots[r]; const float w = wts[r]; unsigned char* rowp = ys + (size_t)slot * D + col0;
; #pragma unroll
;                     for (int bj = 0; bj < 2; ++bj) { const f32x4 v0 = (acc[ai][bj][m][0] * WSCALE_INV + bv[bj][0]) * w, v1 = (acc[ai][bj][m][1] * WSCALE_INV + bv[bj][1]) * w;
;                         u32x2 o; o.x = pk4f8(v0[0], v0[1], v0[2], v0[3]); o.y = pk4f8(v1[0], v1[1], v1[2], v1[3]);
;                         *(u32x2*)(rowp + bj * HALF) = o; } } }
.LBB0_1348:
	s_or_b64 exec, exec, s[2:3]
	v_add_u32_e32 v48, 0x90, v160
	v_cmp_gt_i32_e32 vcc, s30, v48
	s_and_saveexec_b64 s[2:3], vcc
	s_cbranch_execz .LBB0_1350
	v_mov_b32_e32 v48, v180
	v_mov_b32_e32 v50, v181
	v_pk_fma_f32 v[40:41], v[40:41], s[16:17], v[136:137] op_sel_hi:[1,0,1]
	v_pk_fma_f32 v[44:45], v[44:45], s[16:17], v[140:141] op_sel_hi:[1,0,1]
	v_pk_mul_f32 v[40:41], v[40:41], v[50:51] op_sel_hi:[1,0]
	v_pk_mul_f32 v[44:45], v[44:45], v[50:51] op_sel_hi:[1,0]
	v_cvt_pk_fp8_f32 v167, v40, v41
	v_pk_fma_f32 v[40:41], v[42:43], s[16:17], v[138:139] op_sel_hi:[1,0,1]
	v_pk_fma_f32 v[36:37], v[36:37], s[16:17], v[132:133] op_sel_hi:[1,0,1]
	v_pk_mul_f32 v[40:41], v[40:41], v[50:51] op_sel_hi:[1,0]
	v_pk_fma_f32 v[32:33], v[32:33], s[16:17], v[128:129] op_sel_hi:[1,0,1]
	v_cvt_pk_fp8_f32 v166, v44, v45
	v_cvt_pk_fp8_f32 v167, v40, v41 op_sel:[0,0,1]
	v_pk_mul_f32 v[36:37], v[36:37], v[50:51] op_sel_hi:[1,0]
	v_pk_mul_f32 v[32:33], v[32:33], v[50:51] op_sel_hi:[1,0]
	v_cvt_pk_fp8_f32 v168, v36, v37
	v_cvt_pk_fp8_f32 v169, v32, v33
	v_pk_fma_f32 v[46:47], v[46:47], s[16:17], v[142:143] op_sel_hi:[1,0,1]
	v_pk_fma_f32 v[38:39], v[38:39], s[16:17], v[134:135] op_sel_hi:[1,0,1]
	v_pk_mul_f32 v[46:47], v[46:47], v[50:51] op_sel_hi:[1,0]
	v_pk_fma_f32 v[32:33], v[34:35], s[16:17], v[130:131] op_sel_hi:[1,0,1]
	v_ashrrev_i32_e32 v49, 31, v48
	v_cvt_pk_fp8_f32 v166, v46, v47 op_sel:[0,0,1]
	v_pk_mul_f32 v[38:39], v[38:39], v[50:51] op_sel_hi:[1,0]
	v_pk_mul_f32 v[32:33], v[32:33], v[50:51] op_sel_hi:[1,0]
	v_lshlrev_b64 v[48:49], 11, v[48:49]
	v_cvt_pk_fp8_f32 v168, v38, v39 op_sel:[0,0,1]
	v_cvt_pk_fp8_f32 v169, v32, v33 op_sel:[0,0,1]
	v_lshl_add_u64 v[32:33], s[12:13], 0, v[48:49]
	v_lshl_add_u64 v[32:33], v[32:33], 0, v[144:145]
	global_store_dwordx4 v[32:33], v[166:169], off
.LBB0_1350:
	s_or_b64 exec, exec, s[2:3]
	v_add_u32_e32 v32, 0xa0, v160
	v_cmp_gt_i32_e32 vcc, s30, v32
	s_and_saveexec_b64 s[2:3], vcc
	s_cbranch_execz .LBB0_1352
	v_mov_b32_e32 v32, v182
	v_mov_b32_e32 v34, v183
	v_pk_fma_f32 v[24:25], v[24:25], s[16:17], v[136:137] op_sel_hi:[1,0,1]
	v_pk_fma_f32 v[28:29], v[28:29], s[16:17], v[140:141] op_sel_hi:[1,0,1]
	v_pk_mul_f32 v[24:25], v[24:25], v[34:35] op_sel_hi:[1,0]
	v_pk_mul_f32 v[28:29], v[28:29], v[34:35] op_sel_hi:[1,0]
	v_cvt_pk_fp8_f32 v167, v24, v25
	v_pk_fma_f32 v[24:25], v[26:27], s[16:17], v[138:139] op_sel_hi:[1,0,1]
	v_pk_fma_f32 v[20:21], v[20:21], s[16:17], v[132:133] op_sel_hi:[1,0,1]
	v_pk_mul_f32 v[24:25], v[24:25], v[34:35] op_sel_hi:[1,0]
	v_pk_fma_f32 v[16:17], v[16:17], s[16:17], v[128:129] op_sel_hi:[1,0,1]
	v_cvt_pk_fp8_f32 v166, v28, v29
	v_cvt_pk_fp8_f32 v167, v24, v25 op_sel:[0,0,1]
	v_pk_mul_f32 v[20:21], v[20:21], v[34:35] op_sel_hi:[1,0]
	v_pk_mul_f32 v[16:17], v[16:17], v[34:35] op_sel_hi:[1,0]
	v_cvt_pk_fp8_f32 v168, v20, v21
	v_cvt_pk_fp8_f32 v169, v16, v17
	v_pk_fma_f32 v[30:31], v[30:31], s[16:17], v[142:143] op_sel_hi:[1,0,1]
	v_pk_fma_f32 v[22:23], v[22:23], s[16:17], v[134:135] op_sel_hi:[1,0,1]
	v_pk_mul_f32 v[30:31], v[30:31], v[34:35] op_sel_hi:[1,0]
	v_pk_fma_f32 v[16:17], v[18:19], s[16:17], v[130:131] op_sel_hi:[1,0,1]
	v_ashrrev_i32_e32 v33, 31, v32
	v_cvt_pk_fp8_f32 v166, v30, v31 op_sel:[0,0,1]
	v_pk_mul_f32 v[22:23], v[22:23], v[34:35] op_sel_hi:[1,0]
	v_pk_mul_f32 v[16:17], v[16:17], v[34:35] op_sel_hi:[1,0]
	v_lshlrev_b64 v[32:33], 11, v[32:33]
	v_cvt_pk_fp8_f32 v168, v22, v23 op_sel:[0,0,1]
	v_cvt_pk_fp8_f32 v169, v16, v17 op_sel:[0,0,1]
	v_lshl_add_u64 v[16:17], s[12:13], 0, v[32:33]
	v_lshl_add_u64 v[16:17], v[16:17], 0, v[144:145]
	global_store_dwordx4 v[16:17], v[166:169], off
.LBB0_1352:
	s_or_b64 exec, exec, s[2:3]
	v_add_u32_e32 v16, 0xb0, v160
	v_cmp_gt_i32_e32 vcc, s30, v16
	s_and_saveexec_b64 s[2:3], vcc
	s_cbranch_execz .LBB0_1354
	v_mov_b32_e32 v16, v184
	v_mov_b32_e32 v18, v185
	v_pk_fma_f32 v[8:9], v[8:9], s[16:17], v[136:137] op_sel_hi:[1,0,1]
	v_pk_fma_f32 v[12:13], v[12:13], s[16:17], v[140:141] op_sel_hi:[1,0,1]
	v_pk_mul_f32 v[8:9], v[8:9], v[18:19] op_sel_hi:[1,0]
	v_pk_mul_f32 v[12:13], v[12:13], v[18:19] op_sel_hi:[1,0]
	v_cvt_pk_fp8_f32 v167, v8, v9
	v_pk_fma_f32 v[8:9], v[10:11], s[16:17], v[138:139] op_sel_hi:[1,0,1]
	v_pk_fma_f32 v[4:5], v[4:5], s[16:17], v[132:133] op_sel_hi:[1,0,1]
	v_pk_mul_f32 v[8:9], v[8:9], v[18:19] op_sel_hi:[1,0]
	v_pk_fma_f32 v[0:1], v[0:1], s[16:17], v[128:129] op_sel_hi:[1,0,1]
	v_cvt_pk_fp8_f32 v166, v12, v13
	v_cvt_pk_fp8_f32 v167, v8, v9 op_sel:[0,0,1]
	v_pk_mul_f32 v[4:5], v[4:5], v[18:19] op_sel_hi:[1,0]
	v_pk_mul_f32 v[0:1], v[0:1], v[18:19] op_sel_hi:[1,0]
	v_cvt_pk_fp8_f32 v168, v4, v5
	v_cvt_pk_fp8_f32 v169, v0, v1
	v_pk_fma_f32 v[14:15], v[14:15], s[16:17], v[142:143] op_sel_hi:[1,0,1]
	v_pk_fma_f32 v[6:7], v[6:7], s[16:17], v[134:135] op_sel_hi:[1,0,1]
	v_pk_mul_f32 v[14:15], v[14:15], v[18:19] op_sel_hi:[1,0]
	v_pk_fma_f32 v[0:1], v[2:3], s[16:17], v[130:131] op_sel_hi:[1,0,1]
	v_ashrrev_i32_e32 v17, 31, v16
	v_cvt_pk_fp8_f32 v166, v14, v15 op_sel:[0,0,1]
	v_pk_mul_f32 v[6:7], v[6:7], v[18:19] op_sel_hi:[1,0]
	v_pk_mul_f32 v[0:1], v[0:1], v[18:19] op_sel_hi:[1,0]
	v_lshlrev_b64 v[16:17], 11, v[16:17]
	v_cvt_pk_fp8_f32 v168, v6, v7 op_sel:[0,0,1]
	v_cvt_pk_fp8_f32 v169, v0, v1 op_sel:[0,0,1]
	v_lshl_add_u64 v[0:1], s[12:13], 0, v[16:17]
	v_lshl_add_u64 v[0:1], v[0:1], 0, v[144:145]
	global_store_dwordx4 v[0:1], v[166:169], off
